# v28: v27 without the wait-before-stores (prefetch DMAs covered by the counted wait at the next unit's top)
# speedup vs baseline: 1.0030x; 1.0030x over previous
; __device__ __forceinline__ unsigned cvt_pk_bf16(float lo, float hi) { unsigned r; asm volatile("v_cvt_pk_bf16_f32 %0, %1, %2" : "=v"(r) : "v"(lo), "v"(hi)); return r; }
; __device__ __forceinline__ void sg_phase(const Frame& F, const KArgs& a, const int u_first, const int u_count) {
;     ...
; #pragma unroll
;         for (int j = 0; j < 8; ++j) { const int ch = 16 * j + 4 * kq; const u32x2 uu = uraw[j];
;             const float o0 = __builtin_bit_cast(float, uu.x << 16) * (acc[j][0] + bs), o1 = __builtin_bit_cast(float, uu.x & 0xffff0000u) * (acc[j][1] + bs);
;             const float o2 = __builtin_bit_cast(float, uu.y << 16) * (acc[j][2] + bs), o3 = __builtin_bit_cast(float, uu.y & 0xffff0000u) * (acc[j][3] + bs);
;             u32x2 o; o.x = cvt_pk_bf16(o0, o1); o.y = cvt_pk_bf16(o2, o3); *(u32x2*)(AS + (size_t)(t0 + t) * DM + FW + g * 128 + ch) = o; }
;         __syncthreads();
;     }
.LBB0_803:
	s_waitcnt vmcnt(8)
	v_lshlrev_b64 v[34:35], 12, v[174:175]
	v_lshl_add_u64 v[34:35], s[72:73], 0, v[34:35]
	v_lshl_add_u64 v[34:35], v[34:35], 0, s[78:79]
	v_mov_b32_e32 v157, v147
	v_lshl_add_u64 v[34:35], v[34:35], 0, v[156:157]
	s_mov_b64 s[70:71], 0x17800800
	v_lshl_add_u64 v[38:39], v[34:35], 0, s[70:71]
	v_lshl_add_u64 v[38:39], v[38:39], 0, v[156:157]
	v_lshlrev_b32_e32 v34, 16, v170
	v_add_f32_e32 v35, v146, v82
	v_mul_f32_e32 v34, v35, v34
	v_and_b32_e32 v35, 0xffff0000, v170
	v_add_f32_e32 v36, v146, v83
	v_mul_f32_e32 v35, v36, v35
	v_lshlrev_b32_e32 v36, 16, v171
	v_add_f32_e32 v37, v146, v84
	v_mul_f32_e32 v36, v37, v36
	v_and_b32_e32 v37, 0xffff0000, v171
	v_add_f32_e32 v40, v146, v85
	v_mul_f32_e32 v37, v40, v37
	v_cvt_pk_bf16_f32 v170, v34, v35
	v_cvt_pk_bf16_f32 v171, v36, v37
	v_lshlrev_b32_e32 v34, 16, v172
	v_add_f32_e32 v35, v146, v86
	v_mul_f32_e32 v34, v35, v34
	v_and_b32_e32 v35, 0xffff0000, v172
	v_add_f32_e32 v36, v146, v87
	v_mul_f32_e32 v35, v36, v35
	v_lshlrev_b32_e32 v36, 16, v173
	v_add_f32_e32 v37, v146, v88
	v_mul_f32_e32 v36, v37, v36
	v_and_b32_e32 v37, 0xffff0000, v173
	v_add_f32_e32 v40, v146, v89
	v_mul_f32_e32 v37, v40, v37
	v_cvt_pk_bf16_f32 v172, v34, v35
	v_cvt_pk_bf16_f32 v173, v36, v37
	s_nop 0
	global_store_dwordx4 v[38:39], v[170:173], off
	v_lshlrev_b32_e32 v34, 16, v166
	v_add_f32_e32 v35, v146, v74
	v_mul_f32_e32 v34, v35, v34
	v_and_b32_e32 v35, 0xffff0000, v166
	v_add_f32_e32 v36, v146, v75
	v_mul_f32_e32 v35, v36, v35
	v_lshlrev_b32_e32 v36, 16, v167
	v_add_f32_e32 v37, v146, v76
	v_mul_f32_e32 v36, v37, v36
	v_and_b32_e32 v37, 0xffff0000, v167
	v_add_f32_e32 v40, v146, v77
	v_mul_f32_e32 v37, v40, v37
	v_cvt_pk_bf16_f32 v166, v34, v35
	v_cvt_pk_bf16_f32 v167, v36, v37
	v_lshlrev_b32_e32 v34, 16, v168
	v_add_f32_e32 v35, v146, v78
	v_mul_f32_e32 v34, v35, v34
	v_and_b32_e32 v35, 0xffff0000, v168
	v_add_f32_e32 v36, v146, v79
	v_mul_f32_e32 v35, v36, v35
	v_lshlrev_b32_e32 v36, 16, v169
	v_add_f32_e32 v37, v146, v80
	v_mul_f32_e32 v36, v37, v36
	v_and_b32_e32 v37, 0xffff0000, v169
	v_add_f32_e32 v40, v146, v81
	v_mul_f32_e32 v37, v40, v37
	v_cvt_pk_bf16_f32 v168, v34, v35
	v_cvt_pk_bf16_f32 v169, v36, v37
	s_nop 0
	global_store_dwordx4 v[38:39], v[166:169], off offset:64
	v_lshlrev_b32_e32 v34, 16, v162
	v_add_f32_e32 v35, v146, v66
	v_mul_f32_e32 v34, v35, v34
	v_and_b32_e32 v35, 0xffff0000, v162
	v_add_f32_e32 v36, v146, v67
	v_mul_f32_e32 v35, v36, v35
	v_lshlrev_b32_e32 v36, 16, v163
	v_add_f32_e32 v37, v146, v68
	v_mul_f32_e32 v36, v37, v36
	v_and_b32_e32 v37, 0xffff0000, v163
	v_add_f32_e32 v40, v146, v69
	v_mul_f32_e32 v37, v40, v37
	v_cvt_pk_bf16_f32 v162, v34, v35
	v_cvt_pk_bf16_f32 v163, v36, v37
	v_lshlrev_b32_e32 v34, 16, v164
	v_add_f32_e32 v35, v146, v70
	v_mul_f32_e32 v34, v35, v34
	v_and_b32_e32 v35, 0xffff0000, v164
	v_add_f32_e32 v36, v146, v71
	v_mul_f32_e32 v35, v36, v35
	v_lshlrev_b32_e32 v36, 16, v165
	v_add_f32_e32 v37, v146, v72
	v_mul_f32_e32 v36, v37, v36
	v_and_b32_e32 v37, 0xffff0000, v165
	v_add_f32_e32 v40, v146, v73
	v_mul_f32_e32 v37, v40, v37
	v_cvt_pk_bf16_f32 v164, v34, v35
	v_cvt_pk_bf16_f32 v165, v36, v37
	s_nop 0
	global_store_dwordx4 v[38:39], v[162:165], off offset:128
	v_lshlrev_b32_e32 v34, 16, v158
	v_add_f32_e32 v35, v146, v58
	v_mul_f32_e32 v34, v35, v34
	v_and_b32_e32 v35, 0xffff0000, v158
	v_add_f32_e32 v36, v146, v59
	v_mul_f32_e32 v35, v36, v35
	v_lshlrev_b32_e32 v36, 16, v159
	v_add_f32_e32 v37, v146, v60
	v_mul_f32_e32 v36, v37, v36
	v_and_b32_e32 v37, 0xffff0000, v159
	v_add_f32_e32 v40, v146, v61
	v_mul_f32_e32 v37, v40, v37
	v_cvt_pk_bf16_f32 v158, v34, v35
	v_cvt_pk_bf16_f32 v159, v36, v37
	v_lshlrev_b32_e32 v34, 16, v160
	v_add_f32_e32 v35, v146, v62
	v_mul_f32_e32 v34, v35, v34
	v_and_b32_e32 v35, 0xffff0000, v160
	v_add_f32_e32 v36, v146, v63
	v_mul_f32_e32 v35, v36, v35
	v_lshlrev_b32_e32 v36, 16, v161
	v_add_f32_e32 v37, v146, v64
	v_mul_f32_e32 v36, v37, v36
	v_and_b32_e32 v37, 0xffff0000, v161
	v_add_f32_e32 v40, v146, v65
	v_mul_f32_e32 v37, v40, v37
	v_cvt_pk_bf16_f32 v160, v34, v35
	v_cvt_pk_bf16_f32 v161, v36, v37
	s_nop 0
	global_store_dwordx4 v[38:39], v[158:161], off offset:192
	v_add_u32_e32 v1, -1, v1
	v_cmp_ne_u32_e32 vcc, 0, v1
	s_addk_i32 s33, 0x80
	s_and_b64 vcc, exec, vcc
	s_add_i32 s90, s90, 16
	s_barrier
	s_cbranch_vccz .LBB0_820
